# grid barrier: the acquire's L1 invalidate is issued at arrival (nothing of the workgroup touches L1 between arrival and release: sc1 polls and atomics bypass it, other waves sit in s_barrier) instead
# speedup vs baseline: 1.0033x; 1.0009x over previous
.LBB0_80:
	v_mov_b32_e32 v237, 0x43e00000
	v_mov_b32_e32 v238, 0x42800000
	v_mov_b32_e32 v239, 0xf149f2ca
	s_mov_b32 s4, s58
	s_mov_b64 s[40:41], s[54:55]
	s_waitcnt vmcnt(0)
	s_waitcnt lgkmcnt(0)
	s_barrier
	s_mov_b64 s[6:7], exec
	v_readlane_b32 s8, v252, 2
	v_readlane_b32 s9, v252, 3
	s_and_b64 s[8:9], s[6:7], s[8:9]
	s_xor_b64 s[38:39], s[8:9], s[6:7]
	s_mov_b64 exec, s[8:9]
	s_cbranch_execz .LBB0_126
	v_readlane_b32 s5, v254, 58
	s_waitcnt vmcnt(0) expcnt(0) lgkmcnt(0)
	buffer_inv sc1
	s_nop 0
	v_mov_b32_e32 v0, s5
	ds_read_b32 v2, v0
	v_readlane_b32 s5, v254, 59
	s_waitcnt lgkmcnt(0)
	v_cmp_ne_u32_e32 vcc, 0, v2
	v_mov_b32_e32 v0, s5
	ds_read_b32 v0, v0
	s_cbranch_vccnz .LBB0_96
	v_readlane_b32 s6, v252, 0
	v_readlane_b32 s7, v252, 1
	s_load_dwordx2 s[10:11], s[6:7], 0x4
	s_add_u32 s6, s40, 0x1000
	s_addc_u32 s7, s41, 0
	s_add_u32 s8, s40, 0x1100
	s_addc_u32 s9, s41, 0
	s_waitcnt lgkmcnt(0)
	s_mul_i32 s5, s10, s46
	s_add_u32 s10, s40, 0x1200
	s_mul_i32 s5, s5, s11
	s_addc_u32 s11, s41, 0
	s_add_u32 s12, s40, 0x1300
	s_addc_u32 s13, s41, 0
	s_mov_b32 s33, 1
	s_mov_b64 s[14:15], 0
	s_branch .LBB0_85

.LBB0_108:
	s_or_b64 exec, exec, s[8:9]
	s_waitcnt vmcnt(0) lgkmcnt(0)

	s_waitcnt vmcnt(0)

.LBB0_124:
	s_or_b64 exec, exec, s[8:9]
	s_add_i32 s52, s4, 0x900
	s_lshl_b64 s[4:5], s[52:53], 2
	s_add_u32 s4, s40, s4
	s_addc_u32 s5, s41, s5
	v_mov_b64_e32 v[2:3], s[4:5]
	v_mov_b32_e32 v0, 1
	s_waitcnt vmcnt(0) lgkmcnt(0)

	flat_atomic_add v[2:3], v0
	s_waitcnt vmcnt(0)

.LBB0_227:
	s_mov_b64 s[70:71], s[54:55]
	s_mov_b32 s4, s58
	s_waitcnt vmcnt(0)
	s_waitcnt lgkmcnt(0)
	s_barrier
	s_mov_b64 s[6:7], exec
	v_readlane_b32 s8, v252, 2
	v_readlane_b32 s9, v252, 3
	s_and_b64 s[8:9], s[6:7], s[8:9]
	s_xor_b64 s[40:41], s[8:9], s[6:7]
	s_mov_b64 exec, s[8:9]
	s_cbranch_execz .LBB0_272
	v_readlane_b32 s5, v254, 58
	s_waitcnt vmcnt(0) expcnt(0) lgkmcnt(0)
	buffer_inv sc1
	s_nop 0
	v_mov_b32_e32 v0, s5
	ds_read_b32 v2, v0
	v_readlane_b32 s5, v254, 59
	s_waitcnt lgkmcnt(0)
	v_cmp_ne_u32_e32 vcc, 0, v2
	v_mov_b32_e32 v0, s5
	ds_read_b32 v0, v0
	s_cbranch_vccnz .LBB0_242
	v_readlane_b32 s6, v252, 0
	v_readlane_b32 s7, v252, 1
	s_load_dwordx2 s[10:11], s[6:7], 0x4
	s_add_u32 s6, s70, 0x1000
	s_addc_u32 s7, s71, 0
	s_add_u32 s8, s70, 0x1100
	s_addc_u32 s9, s71, 0
	s_waitcnt lgkmcnt(0)
	s_mul_i32 s5, s10, s46
	s_add_u32 s10, s70, 0x1200
	s_mul_i32 s5, s5, s11
	s_addc_u32 s11, s71, 0
	s_add_u32 s12, s70, 0x1300
	s_addc_u32 s13, s71, 0
	s_mov_b32 s33, 1
	s_mov_b64 s[14:15], 0
	s_branch .LBB0_232

.LBB0_270:
	s_or_b64 exec, exec, s[8:9]
	s_add_i32 s52, s4, 0x900
	s_lshl_b64 s[4:5], s[52:53], 2
	s_add_u32 s4, s70, s4
	s_addc_u32 s5, s71, s5
	v_mov_b64_e32 v[2:3], s[4:5]
	v_mov_b32_e32 v0, 1
	s_waitcnt vmcnt(0) lgkmcnt(0)

	flat_atomic_add v[2:3], v0
	s_waitcnt vmcnt(0)

.LBB0_734:
	s_mov_b64 s[40:41], s[54:55]
	s_mov_b32 s4, s58
	s_waitcnt vmcnt(0)
	s_barrier
	s_mov_b64 s[6:7], exec
	v_readlane_b32 s8, v252, 2
	v_readlane_b32 s9, v252, 3
	s_and_b64 s[8:9], s[6:7], s[8:9]
	s_xor_b64 s[38:39], s[8:9], s[6:7]
	s_mov_b64 exec, s[8:9]
	s_cbranch_execz .LBB0_779
	v_readlane_b32 s5, v254, 58
	s_waitcnt vmcnt(0) expcnt(0) lgkmcnt(0)
	buffer_inv sc1
	s_nop 0
	v_mov_b32_e32 v0, s5
	ds_read_b32 v2, v0
	v_readlane_b32 s5, v254, 59
	s_waitcnt lgkmcnt(0)
	v_cmp_ne_u32_e32 vcc, 0, v2
	v_mov_b32_e32 v0, s5
	ds_read_b32 v0, v0
	s_cbranch_vccnz .LBB0_749
	v_readlane_b32 s6, v252, 0
	v_readlane_b32 s7, v252, 1
	s_load_dwordx2 s[10:11], s[6:7], 0x4
	s_add_u32 s6, s40, 0x1000
	s_addc_u32 s7, s41, 0
	s_add_u32 s8, s40, 0x1100
	s_addc_u32 s9, s41, 0
	s_waitcnt lgkmcnt(0)
	s_mul_i32 s5, s10, s46
	s_add_u32 s10, s40, 0x1200
	s_mul_i32 s5, s5, s11
	s_addc_u32 s11, s41, 0
	s_add_u32 s12, s40, 0x1300
	s_addc_u32 s13, s41, 0
	s_mov_b32 s33, 1
	s_mov_b64 s[14:15], 0
	s_branch .LBB0_739

.LBB0_898:
	s_mov_b64 s[40:41], s[54:55]
	s_mov_b32 s4, s58
	s_waitcnt vmcnt(0)
	s_waitcnt lgkmcnt(0)
	s_barrier
	s_mov_b64 s[6:7], exec
	v_readlane_b32 s8, v252, 2
	v_readlane_b32 s9, v252, 3
	s_and_b64 s[8:9], s[6:7], s[8:9]
	s_mov_b64 exec, s[8:9]
	s_cbranch_execz .LBB0_942
	v_readlane_b32 s5, v254, 58
	s_waitcnt vmcnt(0) expcnt(0) lgkmcnt(0)
	buffer_inv sc1
	s_nop 0
	v_mov_b32_e32 v0, s5
	ds_read_b32 v2, v0
	v_readlane_b32 s5, v254, 59
	s_waitcnt lgkmcnt(0)
	v_cmp_ne_u32_e32 vcc, 0, v2
	v_mov_b32_e32 v0, s5
	ds_read_b32 v0, v0
	s_cbranch_vccnz .LBB0_913
	v_readlane_b32 s8, v252, 0
	v_readlane_b32 s9, v252, 1
	s_load_dwordx2 s[12:13], s[8:9], 0x4
	s_add_u32 s8, s40, 0x1000
	s_addc_u32 s9, s41, 0
	s_add_u32 s10, s40, 0x1100
	s_addc_u32 s11, s41, 0
	s_waitcnt lgkmcnt(0)
	s_mul_i32 s5, s12, s46
	s_add_u32 s12, s40, 0x1200
	s_mul_i32 s5, s5, s13
	s_addc_u32 s13, s41, 0
	s_add_u32 s14, s40, 0x1300
	s_addc_u32 s15, s41, 0
	s_mov_b32 s33, 1
	s_mov_b64 s[16:17], 0
	s_branch .LBB0_903

.LBB0_925:
	s_or_b64 exec, exec, s[10:11]
	s_waitcnt vmcnt(0) lgkmcnt(0)

	s_waitcnt vmcnt(0)

.LBB0_1024:
	s_mov_b64 s[40:41], s[54:55]
	s_mov_b32 s4, s58
	s_waitcnt vmcnt(0)
	s_barrier
	s_mov_b64 s[6:7], exec
	v_readlane_b32 s8, v252, 2
	v_readlane_b32 s9, v252, 3
	s_and_b64 s[8:9], s[6:7], s[8:9]
	s_xor_b64 s[6:7], s[8:9], s[6:7]
	s_mov_b64 exec, s[8:9]
	s_cbranch_execz .LBB0_1069
	v_readlane_b32 s5, v254, 58
	s_waitcnt vmcnt(0) expcnt(0) lgkmcnt(0)
	buffer_inv sc1
	s_nop 0
	v_mov_b32_e32 v0, s5
	ds_read_b32 v2, v0
	v_readlane_b32 s5, v254, 59
	s_waitcnt lgkmcnt(0)
	v_cmp_ne_u32_e32 vcc, 0, v2
	v_mov_b32_e32 v0, s5
	ds_read_b32 v0, v0
	s_cbranch_vccnz .LBB0_1039
	v_readlane_b32 s8, v252, 0
	v_readlane_b32 s9, v252, 1
	s_load_dwordx2 s[12:13], s[8:9], 0x4
	s_add_u32 s8, s40, 0x1000
	s_addc_u32 s9, s41, 0
	s_add_u32 s10, s40, 0x1100
	s_addc_u32 s11, s41, 0
	s_waitcnt lgkmcnt(0)
	s_mul_i32 s5, s12, s46
	s_add_u32 s12, s40, 0x1200
	s_mul_i32 s5, s5, s13
	s_addc_u32 s13, s41, 0
	s_add_u32 s14, s40, 0x1300
	s_addc_u32 s15, s41, 0
	s_mov_b32 s33, 1
	s_mov_b64 s[16:17], 0
	s_branch .LBB0_1029

.LBB0_1067:
	s_or_b64 exec, exec, s[10:11]
	s_addk_i32 s4, 0x900
	s_mov_b32 s5, s53
	s_lshl_b64 s[4:5], s[4:5], 2
	s_add_u32 s4, s40, s4
	s_addc_u32 s5, s41, s5
	v_mov_b64_e32 v[2:3], s[4:5]
	v_mov_b32_e32 v0, 1
	s_waitcnt vmcnt(0) lgkmcnt(0)

	flat_atomic_add v[2:3], v0
	s_waitcnt vmcnt(0)

.Lsc_exit:
.LBB0_1114:
	s_mov_b64 s[70:71], s[54:55]
	s_mov_b32 s4, s58
	s_waitcnt vmcnt(0)
	s_barrier
	s_mov_b64 s[6:7], exec
	v_readlane_b32 s8, v252, 2
	v_readlane_b32 s9, v252, 3
	s_and_b64 s[8:9], s[6:7], s[8:9]
	s_xor_b64 s[40:41], s[8:9], s[6:7]
	s_mov_b64 exec, s[8:9]
	s_cbranch_execz .LBB0_1159
	v_readlane_b32 s5, v254, 58
	s_waitcnt vmcnt(0) expcnt(0) lgkmcnt(0)
	buffer_inv sc1
	s_nop 0
	v_mov_b32_e32 v0, s5
	ds_read_b32 v2, v0
	v_readlane_b32 s5, v254, 59
	s_waitcnt lgkmcnt(0)
	v_cmp_ne_u32_e32 vcc, 0, v2
	v_mov_b32_e32 v0, s5
	ds_read_b32 v0, v0
	s_cbranch_vccnz .LBB0_1129
	v_readlane_b32 s8, v252, 0
	v_readlane_b32 s9, v252, 1
	s_load_dwordx2 s[6:7], s[8:9], 0x4
	s_add_u32 s8, s70, 0x1000
	s_addc_u32 s9, s71, 0
	s_add_u32 s10, s70, 0x1100
	s_addc_u32 s11, s71, 0
	s_add_u32 s12, s70, 0x1200
	s_addc_u32 s13, s71, 0
	s_waitcnt lgkmcnt(0)
	s_mul_i32 s5, s6, s46
	s_add_u32 s14, s70, 0x1300
	s_mul_i32 s5, s5, s7
	s_addc_u32 s15, s71, 0
	s_mov_b32 s6, 1
	s_mov_b64 s[16:17], 0
	s_branch .LBB0_1119

.LBB0_1157:
	s_or_b64 exec, exec, s[10:11]
	s_add_i32 s52, s4, 0x900
	s_lshl_b64 s[4:5], s[52:53], 2
	s_add_u32 s4, s70, s4
	s_addc_u32 s5, s71, s5
	v_mov_b64_e32 v[2:3], s[4:5]
	v_mov_b32_e32 v0, 1
	s_waitcnt vmcnt(0) lgkmcnt(0)

	flat_atomic_add v[2:3], v0
	s_waitcnt vmcnt(0)

.LBB0_1181:
	s_mov_b64 s[70:71], s[54:55]
	s_mov_b32 s4, s58
	s_waitcnt vmcnt(0)
	s_barrier
	s_mov_b64 s[6:7], exec
	v_readlane_b32 s8, v252, 2
	v_readlane_b32 s9, v252, 3
	s_and_b64 s[8:9], s[6:7], s[8:9]
	s_xor_b64 s[40:41], s[8:9], s[6:7]
	s_mov_b64 exec, s[8:9]
	s_cbranch_execz .LBB0_1226
	v_readlane_b32 s5, v254, 58
	s_waitcnt vmcnt(0) expcnt(0) lgkmcnt(0)
	buffer_inv sc1
	s_nop 0
	v_mov_b32_e32 v0, s5
	ds_read_b32 v2, v0
	v_readlane_b32 s5, v254, 59
	s_waitcnt lgkmcnt(0)
	v_cmp_ne_u32_e32 vcc, 0, v2
	v_mov_b32_e32 v0, s5
	ds_read_b32 v0, v0
	s_cbranch_vccnz .LBB0_1196
	v_readlane_b32 s8, v252, 0
	v_readlane_b32 s9, v252, 1
	s_load_dwordx2 s[6:7], s[8:9], 0x4
	s_add_u32 s8, s70, 0x1000
	s_addc_u32 s9, s71, 0
	s_add_u32 s10, s70, 0x1100
	s_addc_u32 s11, s71, 0
	s_add_u32 s12, s70, 0x1200
	s_addc_u32 s13, s71, 0
	s_waitcnt lgkmcnt(0)
	s_mul_i32 s5, s6, s46
	s_add_u32 s14, s70, 0x1300
	s_mul_i32 s5, s5, s7
	s_addc_u32 s15, s71, 0
	s_mov_b32 s6, 1
	s_mov_b64 s[16:17], 0
	s_branch .LBB0_1186

.LBB0_1317:
	s_mov_b64 s[40:41], s[54:55]
	s_mov_b32 s4, s58
	s_waitcnt vmcnt(0)
	s_barrier
	s_mov_b64 s[6:7], exec
	v_readlane_b32 s8, v252, 2
	v_readlane_b32 s9, v252, 3
	s_and_b64 s[8:9], s[6:7], s[8:9]
	v_readlane_b32 s62, v255, 11
	s_xor_b64 s[6:7], s[8:9], s[6:7]
	v_readlane_b32 s63, v255, 12
	s_mov_b64 exec, s[8:9]
	s_cbranch_execz .LBB0_1362
	v_readlane_b32 s5, v254, 58
	s_waitcnt vmcnt(0) expcnt(0) lgkmcnt(0)
	buffer_inv sc1
	s_nop 0
	v_mov_b32_e32 v0, s5
	ds_read_b32 v2, v0
	v_readlane_b32 s5, v254, 59
	s_waitcnt lgkmcnt(0)
	v_cmp_ne_u32_e32 vcc, 0, v2
	v_mov_b32_e32 v0, s5
	ds_read_b32 v0, v0
	s_cbranch_vccnz .LBB0_1332
	v_readlane_b32 s8, v252, 0
	v_readlane_b32 s9, v252, 1
	s_load_dwordx2 s[12:13], s[8:9], 0x4
	s_add_u32 s8, s40, 0x1000
	s_addc_u32 s9, s41, 0
	s_add_u32 s10, s40, 0x1100
	s_addc_u32 s11, s41, 0
	s_waitcnt lgkmcnt(0)
	s_mul_i32 s5, s12, s46
	s_add_u32 s12, s40, 0x1200
	s_mul_i32 s5, s5, s13
	s_addc_u32 s13, s41, 0
	s_add_u32 s14, s40, 0x1300
	s_addc_u32 s15, s41, 0
	s_mov_b32 s33, 1
	s_mov_b64 s[16:17], 0
	s_branch .LBB0_1322

.LBB0_1360:
	s_or_b64 exec, exec, s[10:11]
	s_add_i32 s52, s4, 0x900
	s_lshl_b64 s[4:5], s[52:53], 2
	s_add_u32 s4, s40, s4
	s_addc_u32 s5, s41, s5
	v_mov_b64_e32 v[2:3], s[4:5]
	v_mov_b32_e32 v0, 1
	s_waitcnt vmcnt(0) lgkmcnt(0)

	flat_atomic_add v[2:3], v0
	s_waitcnt vmcnt(0)

.LBB0_1412:
	s_mov_b32 s4, s58
	s_mov_b64 s[40:41], s[54:55]
	s_waitcnt vmcnt(0)
	s_barrier
	s_mov_b64 s[6:7], exec
	v_readlane_b32 s8, v252, 2
	v_readlane_b32 s9, v252, 3
	s_and_b64 s[8:9], s[6:7], s[8:9]
	s_xor_b64 s[6:7], s[8:9], s[6:7]
	s_mov_b64 exec, s[8:9]
	s_cbranch_execz .LBB0_1457
	v_readlane_b32 s5, v254, 58
	s_waitcnt vmcnt(0) expcnt(0) lgkmcnt(0)
	buffer_inv sc1
	s_nop 0
	v_mov_b32_e32 v0, s5
	ds_read_b32 v2, v0
	v_readlane_b32 s5, v254, 59
	s_waitcnt lgkmcnt(0)
	v_cmp_ne_u32_e32 vcc, 0, v2
	v_mov_b32_e32 v0, s5
	ds_read_b32 v0, v0
	s_cbranch_vccnz .LBB0_1427
	v_readlane_b32 s8, v252, 0
	v_readlane_b32 s9, v252, 1
	s_load_dwordx2 s[12:13], s[8:9], 0x4
	s_add_u32 s8, s40, 0x1000
	s_addc_u32 s9, s41, 0
	s_add_u32 s10, s40, 0x1100
	s_addc_u32 s11, s41, 0
	s_waitcnt lgkmcnt(0)
	s_mul_i32 s5, s12, s46
	s_add_u32 s12, s40, 0x1200
	s_mul_i32 s5, s5, s13
	s_addc_u32 s13, s41, 0
	s_add_u32 s14, s40, 0x1300
	s_addc_u32 s15, s41, 0
	s_mov_b32 s33, 1
	s_mov_b64 s[16:17], 0
	s_branch .LBB0_1417

.LBB0_1509:
	v_readlane_b32 s5, v254, 58
	s_waitcnt vmcnt(0) expcnt(0) lgkmcnt(0)
	buffer_inv sc1
	s_nop 0
	v_mov_b32_e32 v0, s5
	ds_read_b32 v2, v0
	v_readlane_b32 s5, v254, 59
	s_waitcnt lgkmcnt(0)
	v_cmp_ne_u32_e32 vcc, 0, v2
	v_mov_b32_e32 v0, s5
	ds_read_b32 v0, v0
	s_cbranch_vccnz .LBB0_1523
	v_readlane_b32 s6, v252, 0
	v_readlane_b32 s7, v252, 1
	s_load_dwordx2 s[10:11], s[6:7], 0x4
	s_add_u32 s6, s40, 0x1000
	s_addc_u32 s7, s41, 0
	s_add_u32 s8, s40, 0x1100
	s_addc_u32 s9, s41, 0
	s_waitcnt lgkmcnt(0)
	s_mul_i32 s5, s10, s46
	s_add_u32 s10, s40, 0x1200
	s_mul_i32 s5, s5, s11
	s_addc_u32 s11, s41, 0
	s_add_u32 s12, s40, 0x1300
	s_addc_u32 s13, s41, 0
	s_mov_b32 s33, 1
	s_mov_b64 s[14:15], 0
	s_branch .LBB0_1513
